# v10 plus sc1 nt on the expert-GEMM output stores (ACT8, Y2)
# baseline (speedup 1.0000x reference)
.LBB0_1182:
	s_lshl_b32 s8, s31, 10
	s_and_b32 s8, s8, 0x400
	v_add_u32_e32 v8, s8, v218
	ds_read_b128 v[14:17], v8
	v_lshl_add_u32 v2, s30, 8, v219
	v_ashrrev_i32_e32 v3, 31, v2
	v_lshlrev_b64 v[2:3], 11, v[2:3]
	s_lshl_b32 s8, s16, 7
	s_waitcnt lgkmcnt(0)
	v_fmamk_f32 v9, v194, 0x39000000, v14
	v_min_f32_e32 v20, 0x40e00000, v9
	v_mul_f32_e32 v9, 0xc01d265f, v20
	v_exp_f32_e32 v21, v9
	v_lshl_add_u64 v[2:3], s[42:43], 0, v[2:3]
	s_and_b32 s16, s8, 0x780
	v_lshl_add_u64 v[2:3], v[2:3], 0, s[16:17]
	v_fmamk_f32 v23, v195, 0x39000000, v15
	v_lshl_add_u64 v[6:7], v[2:3], 0, s[40:41]
	ds_read_b128 v[10:13], v8 offset:512
	ds_read_b128 v[2:5], v8 offset:16
	v_min_f32_e32 v23, 0x40e00000, v23
	v_add_f32_e32 v21, 1.0, v21
	v_mul_f32_e32 v24, 0xc01d265f, v23
	v_rcp_f32_e32 v21, v21
	v_exp_f32_e32 v24, v24
	s_waitcnt lgkmcnt(0)
	v_fmamk_f32 v22, v190, 0x39000000, v10
	v_med3_f32 v22, v22, s87, v224
	v_mul_f32_e32 v20, v20, v21
	v_fma_f32 v21, v22, 4.0, 4.0
	v_add_f32_e32 v22, 1.0, v24
	v_rcp_f32_e32 v22, v22
	v_fmamk_f32 v25, v197, 0x39000000, v17
	v_min_f32_e32 v25, 0x40e00000, v25
	v_mul_f32_e32 v26, 0xc01d265f, v25
	v_mul_f32_e32 v22, v23, v22
	v_fmamk_f32 v23, v196, 0x39000000, v16
	v_min_f32_e32 v23, 0x40e00000, v23
	v_mul_f32_e32 v24, 0xc01d265f, v23
	v_exp_f32_e32 v24, v24
	v_exp_f32_e32 v26, v26
	v_mul_f32_e32 v21, v21, v20
	v_fmamk_f32 v20, v191, 0x39000000, v11
	v_add_f32_e32 v24, 1.0, v24
	v_rcp_f32_e32 v24, v24
	v_med3_f32 v20, v20, s87, v224
	v_fma_f32 v20, v20, 4.0, 4.0
	v_mul_f32_e32 v22, v20, v22
	v_fmamk_f32 v20, v192, 0x39000000, v12
	v_mul_f32_e32 v23, v23, v24
	v_add_f32_e32 v24, 1.0, v26
	v_med3_f32 v20, v20, s87, v224
	v_rcp_f32_e32 v24, v24
	v_fma_f32 v20, v20, 4.0, 4.0
	v_mul_f32_e32 v23, v20, v23
	v_fmamk_f32 v20, v193, 0x39000000, v13
	v_med3_f32 v20, v20, s87, v224
	v_mul_f32_e32 v24, v25, v24
	v_fma_f32 v25, v20, 4.0, 4.0
	v_mov_b32_e32 v20, 0
	v_cvt_pk_fp8_f32 v20, v21, v22
	v_fmamk_f32 v21, v186, 0x39000000, v2
	v_min_f32_e32 v21, 0x40e00000, v21
	v_mul_f32_e32 v22, 0xc01d265f, v21
	v_exp_f32_e32 v22, v22
	v_mul_f32_e32 v24, v25, v24
	v_lshl_add_u64 v[18:19], v[6:7], 0, v[206:207]
	ds_read_b128 v[6:9], v8 offset:528
	v_cvt_pk_fp8_f32 v20, v23, v24 op_sel:[0,0,1]
	v_fmamk_f32 v24, v187, 0x39000000, v3
	v_min_f32_e32 v24, 0x40e00000, v24
	v_add_f32_e32 v22, 1.0, v22
	v_mul_f32_e32 v25, 0xc01d265f, v24
	v_rcp_f32_e32 v22, v22
	v_exp_f32_e32 v25, v25
	s_waitcnt lgkmcnt(0)
	v_fmamk_f32 v23, v182, 0x39000000, v6
	v_med3_f32 v23, v23, s87, v224
	v_mul_f32_e32 v21, v21, v22
	v_fma_f32 v22, v23, 4.0, 4.0
	v_add_f32_e32 v23, 1.0, v25
	v_rcp_f32_e32 v23, v23
	v_fmamk_f32 v26, v189, 0x39000000, v5
	v_min_f32_e32 v26, 0x40e00000, v26
	v_mul_f32_e32 v27, 0xc01d265f, v26
	v_mul_f32_e32 v23, v24, v23
	v_fmamk_f32 v24, v188, 0x39000000, v4
	v_min_f32_e32 v24, 0x40e00000, v24
	v_mul_f32_e32 v25, 0xc01d265f, v24
	v_exp_f32_e32 v25, v25
	v_exp_f32_e32 v27, v27
	v_mul_f32_e32 v22, v22, v21
	v_fmamk_f32 v21, v183, 0x39000000, v7
	v_add_f32_e32 v25, 1.0, v25
	v_rcp_f32_e32 v25, v25
	v_med3_f32 v21, v21, s87, v224
	v_fma_f32 v21, v21, 4.0, 4.0
	v_mul_f32_e32 v23, v21, v23
	v_fmamk_f32 v21, v184, 0x39000000, v8
	v_mul_f32_e32 v24, v24, v25
	v_add_f32_e32 v25, 1.0, v27
	v_med3_f32 v21, v21, s87, v224
	v_rcp_f32_e32 v25, v25
	v_fma_f32 v21, v21, 4.0, 4.0
	v_mul_f32_e32 v24, v21, v24
	v_fmamk_f32 v21, v185, 0x39000000, v9
	v_med3_f32 v21, v21, s87, v224
	v_mul_f32_e32 v25, v26, v25
	v_fma_f32 v26, v21, 4.0, 4.0
	v_mov_b32_e32 v21, 0
	v_cvt_pk_fp8_f32 v21, v22, v23
	v_fmamk_f32 v22, v178, 0x39000000, v14
	v_min_f32_e32 v22, 0x40e00000, v22
	v_mul_f32_e32 v23, 0xc01d265f, v22
	v_exp_f32_e32 v23, v23
	v_mul_f32_e32 v25, v26, v25
	v_cvt_pk_fp8_f32 v21, v24, v25 op_sel:[0,0,1]
	v_fmamk_f32 v25, v179, 0x39000000, v15
	v_min_f32_e32 v25, 0x40e00000, v25
	v_add_f32_e32 v23, 1.0, v23
	v_mul_f32_e32 v26, 0xc01d265f, v25
	v_rcp_f32_e32 v23, v23
	v_exp_f32_e32 v26, v26
	v_fmamk_f32 v24, v174, 0x39000000, v10
	v_med3_f32 v24, v24, s87, v224
	v_mul_f32_e32 v22, v22, v23
	v_fma_f32 v23, v24, 4.0, 4.0
	v_add_f32_e32 v24, 1.0, v26
	v_rcp_f32_e32 v24, v24
	v_fmamk_f32 v27, v181, 0x39000000, v17
	v_min_f32_e32 v27, 0x40e00000, v27
	v_mul_f32_e32 v28, 0xc01d265f, v27
	v_mul_f32_e32 v24, v25, v24
	v_fmamk_f32 v25, v180, 0x39000000, v16
	v_min_f32_e32 v25, 0x40e00000, v25
	v_mul_f32_e32 v26, 0xc01d265f, v25
	v_exp_f32_e32 v26, v26
	v_exp_f32_e32 v28, v28
	v_mul_f32_e32 v23, v23, v22
	v_fmamk_f32 v22, v175, 0x39000000, v11
	v_add_f32_e32 v26, 1.0, v26
	v_rcp_f32_e32 v26, v26
	v_med3_f32 v22, v22, s87, v224
	v_fma_f32 v22, v22, 4.0, 4.0
	v_mul_f32_e32 v24, v22, v24
	v_fmamk_f32 v22, v176, 0x39000000, v12
	v_mul_f32_e32 v25, v25, v26
	v_add_f32_e32 v26, 1.0, v28
	v_med3_f32 v22, v22, s87, v224
	v_rcp_f32_e32 v26, v26
	v_fma_f32 v22, v22, 4.0, 4.0
	v_mul_f32_e32 v25, v22, v25
	v_fmamk_f32 v22, v177, 0x39000000, v13
	v_med3_f32 v22, v22, s87, v224
	v_mul_f32_e32 v26, v27, v26
	v_fma_f32 v27, v22, 4.0, 4.0
	v_fmamk_f32 v22, v170, 0x39000000, v2
	v_min_f32_e32 v28, 0x40e00000, v22
	v_mul_f32_e32 v22, 0xc01d265f, v28
	v_exp_f32_e32 v29, v22
	v_mov_b32_e32 v22, 0
	v_cvt_pk_fp8_f32 v22, v23, v24
	v_mul_f32_e32 v23, v27, v26
	v_add_f32_e32 v24, 1.0, v29
	v_rcp_f32_e32 v24, v24
	v_cvt_pk_fp8_f32 v22, v25, v23 op_sel:[0,0,1]
	v_fmamk_f32 v25, v171, 0x39000000, v3
	v_min_f32_e32 v25, 0x40e00000, v25
	v_mul_f32_e32 v26, 0xc01d265f, v25
	v_exp_f32_e32 v26, v26
	v_fmamk_f32 v27, v172, 0x39000000, v4
	v_min_f32_e32 v27, 0x40e00000, v27
	v_mul_f32_e32 v24, v28, v24
	v_add_f32_e32 v26, 1.0, v26
	v_mul_f32_e32 v28, 0xc01d265f, v27
	v_rcp_f32_e32 v26, v26
	v_exp_f32_e32 v28, v28
	v_fmamk_f32 v23, v166, 0x39000000, v6
	v_med3_f32 v23, v23, s87, v224
	v_mul_f32_e32 v25, v25, v26
	v_add_f32_e32 v26, 1.0, v28
	v_rcp_f32_e32 v26, v26
	v_fma_f32 v23, v23, 4.0, 4.0
	v_mul_f32_e32 v24, v23, v24
	v_fmamk_f32 v23, v167, 0x39000000, v7
	v_mul_f32_e32 v26, v27, v26
	v_fmamk_f32 v27, v173, 0x39000000, v5
	v_min_f32_e32 v27, 0x40e00000, v27
	v_mul_f32_e32 v28, 0xc01d265f, v27
	v_med3_f32 v23, v23, s87, v224
	v_exp_f32_e32 v28, v28
	v_fma_f32 v23, v23, 4.0, 4.0
	v_mul_f32_e32 v25, v23, v25
	v_fmamk_f32 v23, v168, 0x39000000, v8
	v_med3_f32 v23, v23, s87, v224
	v_fma_f32 v23, v23, 4.0, 4.0
	v_add_f32_e32 v28, 1.0, v28
	v_mul_f32_e32 v26, v23, v26
	v_fmamk_f32 v23, v169, 0x39000000, v9
	v_rcp_f32_e32 v28, v28
	v_med3_f32 v29, v23, s87, v224
	v_mov_b32_e32 v23, 0
	v_cvt_pk_fp8_f32 v23, v24, v25
	v_mul_f32_e32 v24, v27, v28
	v_fma_f32 v25, v29, 4.0, 4.0
	v_mul_f32_e32 v24, v25, v24
	v_cvt_pk_fp8_f32 v23, v26, v24 op_sel:[0,0,1]
	v_permlane16_swap_b32_e32 v20, v22
	v_fmamk_f32 v24, v162, 0x39000000, v14
	v_permlane16_swap_b32_e32 v21, v23
	global_store_dwordx4 v[18:19], v[20:23], off sc1 nt
	v_min_f32_e32 v24, 0x40e00000, v24
	v_mul_f32_e32 v25, 0xc01d265f, v24
	v_fmamk_f32 v22, v163, 0x39000000, v15
	v_min_f32_e32 v22, 0x40e00000, v22
	v_mul_f32_e32 v23, 0xc01d265f, v22
	v_exp_f32_e32 v23, v23
	v_exp_f32_e32 v25, v25
	v_fmamk_f32 v20, v158, 0x39000000, v10
	v_med3_f32 v20, v20, s87, v224
	v_add_f32_e32 v23, 1.0, v23
	v_rcp_f32_e32 v23, v23
	v_add_f32_e32 v21, 1.0, v25
	v_rcp_f32_e32 v21, v21
	v_fmamk_f32 v25, v165, 0x39000000, v17
	v_mul_f32_e32 v22, v22, v23
	v_fmamk_f32 v23, v164, 0x39000000, v16
	v_min_f32_e32 v23, 0x40e00000, v23
	v_mul_f32_e32 v21, v24, v21
	v_mul_f32_e32 v24, 0xc01d265f, v23
	v_exp_f32_e32 v24, v24
	v_min_f32_e32 v25, 0x40e00000, v25
	v_mul_f32_e32 v26, 0xc01d265f, v25
	v_fma_f32 v20, v20, 4.0, 4.0
	v_add_f32_e32 v24, 1.0, v24
	v_rcp_f32_e32 v24, v24
	v_exp_f32_e32 v26, v26
	v_mul_f32_e32 v21, v20, v21
	v_fmamk_f32 v20, v159, 0x39000000, v11
	v_med3_f32 v20, v20, s87, v224
	v_fma_f32 v20, v20, 4.0, 4.0
	v_mul_f32_e32 v22, v20, v22
	v_fmamk_f32 v20, v160, 0x39000000, v12
	v_mul_f32_e32 v23, v23, v24
	v_add_f32_e32 v24, 1.0, v26
	v_med3_f32 v20, v20, s87, v224
	v_rcp_f32_e32 v24, v24
	v_fma_f32 v20, v20, 4.0, 4.0
	v_mul_f32_e32 v23, v20, v23
	v_fmamk_f32 v20, v161, 0x39000000, v13
	v_med3_f32 v20, v20, s87, v224
	v_mul_f32_e32 v24, v25, v24
	v_fma_f32 v25, v20, 4.0, 4.0
	v_mov_b32_e32 v20, 0
	v_cvt_pk_fp8_f32 v20, v21, v22
	v_fmamk_f32 v21, v154, 0x39000000, v2
	v_min_f32_e32 v21, 0x40e00000, v21
	v_mul_f32_e32 v22, 0xc01d265f, v21
	v_exp_f32_e32 v22, v22
	v_mul_f32_e32 v24, v25, v24
	v_cvt_pk_fp8_f32 v20, v23, v24 op_sel:[0,0,1]
	v_fmamk_f32 v24, v155, 0x39000000, v3
	v_min_f32_e32 v24, 0x40e00000, v24
	v_add_f32_e32 v22, 1.0, v22
	v_mul_f32_e32 v25, 0xc01d265f, v24
	v_rcp_f32_e32 v22, v22
	v_exp_f32_e32 v25, v25
	v_fmamk_f32 v23, v150, 0x39000000, v6
	v_med3_f32 v23, v23, s87, v224
	v_mul_f32_e32 v21, v21, v22
	v_fma_f32 v22, v23, 4.0, 4.0
	v_add_f32_e32 v23, 1.0, v25
	v_rcp_f32_e32 v23, v23
	v_fmamk_f32 v26, v157, 0x39000000, v5
	v_min_f32_e32 v26, 0x40e00000, v26
	v_mul_f32_e32 v27, 0xc01d265f, v26
	v_mul_f32_e32 v23, v24, v23
	v_fmamk_f32 v24, v156, 0x39000000, v4
	v_min_f32_e32 v24, 0x40e00000, v24
	v_mul_f32_e32 v25, 0xc01d265f, v24
	v_exp_f32_e32 v25, v25
	v_exp_f32_e32 v27, v27
	v_mul_f32_e32 v22, v22, v21
	v_fmamk_f32 v21, v151, 0x39000000, v7
	v_add_f32_e32 v25, 1.0, v25
	v_rcp_f32_e32 v25, v25
	v_med3_f32 v21, v21, s87, v224
	v_fma_f32 v21, v21, 4.0, 4.0
	v_mul_f32_e32 v23, v21, v23
	v_fmamk_f32 v21, v152, 0x39000000, v8
	v_mul_f32_e32 v24, v24, v25
	v_add_f32_e32 v25, 1.0, v27
	v_med3_f32 v21, v21, s87, v224
	v_rcp_f32_e32 v25, v25
	v_fma_f32 v21, v21, 4.0, 4.0
	v_mul_f32_e32 v24, v21, v24
	v_fmamk_f32 v21, v153, 0x39000000, v9
	v_med3_f32 v21, v21, s87, v224
	v_mul_f32_e32 v25, v26, v25
	v_fma_f32 v26, v21, 4.0, 4.0
	v_mov_b32_e32 v21, 0
	v_cvt_pk_fp8_f32 v21, v22, v23
	v_fmamk_f32 v22, v146, 0x39000000, v14
	v_min_f32_e32 v22, 0x40e00000, v22
	v_mul_f32_e32 v23, 0xc01d265f, v22
	v_exp_f32_e32 v23, v23
	v_mul_f32_e32 v25, v26, v25
	v_cvt_pk_fp8_f32 v21, v24, v25 op_sel:[0,0,1]
	v_fmamk_f32 v25, v147, 0x39000000, v15
	v_min_f32_e32 v25, 0x40e00000, v25
	v_add_f32_e32 v23, 1.0, v23
	v_mul_f32_e32 v26, 0xc01d265f, v25
	v_rcp_f32_e32 v23, v23
	v_exp_f32_e32 v26, v26
	v_fmamk_f32 v24, v142, 0x39000000, v10
	v_med3_f32 v24, v24, s87, v224
	v_mul_f32_e32 v22, v22, v23
	v_fma_f32 v23, v24, 4.0, 4.0
	v_add_f32_e32 v24, 1.0, v26
	v_rcp_f32_e32 v24, v24
	v_fmamk_f32 v27, v149, 0x39000000, v17
	v_min_f32_e32 v27, 0x40e00000, v27
	v_mul_f32_e32 v28, 0xc01d265f, v27
	v_mul_f32_e32 v24, v25, v24
	v_fmamk_f32 v25, v148, 0x39000000, v16
	v_min_f32_e32 v25, 0x40e00000, v25
	v_mul_f32_e32 v26, 0xc01d265f, v25
	v_exp_f32_e32 v26, v26
	v_exp_f32_e32 v28, v28
	v_mul_f32_e32 v23, v23, v22
	v_fmamk_f32 v22, v143, 0x39000000, v11
	v_add_f32_e32 v26, 1.0, v26
	v_rcp_f32_e32 v26, v26
	v_med3_f32 v22, v22, s87, v224
	v_fma_f32 v22, v22, 4.0, 4.0
	v_mul_f32_e32 v24, v22, v24
	v_fmamk_f32 v22, v144, 0x39000000, v12
	v_mul_f32_e32 v25, v25, v26
	v_add_f32_e32 v26, 1.0, v28
	v_med3_f32 v22, v22, s87, v224
	v_rcp_f32_e32 v26, v26
	v_fma_f32 v22, v22, 4.0, 4.0
	v_mul_f32_e32 v25, v22, v25
	v_fmamk_f32 v22, v145, 0x39000000, v13
	v_med3_f32 v22, v22, s87, v224
	v_mul_f32_e32 v26, v27, v26
	v_fma_f32 v27, v22, 4.0, 4.0
	v_fmamk_f32 v22, v138, 0x39000000, v2
	v_min_f32_e32 v28, 0x40e00000, v22
	v_mul_f32_e32 v22, 0xc01d265f, v28
	v_exp_f32_e32 v29, v22
	v_mov_b32_e32 v22, 0
	v_cvt_pk_fp8_f32 v22, v23, v24
	v_mul_f32_e32 v23, v27, v26
	v_add_f32_e32 v24, 1.0, v29
	v_rcp_f32_e32 v24, v24
	v_cvt_pk_fp8_f32 v22, v25, v23 op_sel:[0,0,1]
	v_fmamk_f32 v25, v139, 0x39000000, v3
	v_min_f32_e32 v25, 0x40e00000, v25
	v_mul_f32_e32 v26, 0xc01d265f, v25
	v_exp_f32_e32 v26, v26
	v_fmamk_f32 v27, v140, 0x39000000, v4
	v_min_f32_e32 v27, 0x40e00000, v27
	v_mul_f32_e32 v24, v28, v24
	v_add_f32_e32 v26, 1.0, v26
	v_mul_f32_e32 v28, 0xc01d265f, v27
	v_rcp_f32_e32 v26, v26
	v_exp_f32_e32 v28, v28
	v_fmamk_f32 v23, v134, 0x39000000, v6
	v_med3_f32 v23, v23, s87, v224
	v_mul_f32_e32 v25, v25, v26
	v_add_f32_e32 v26, 1.0, v28
	v_rcp_f32_e32 v26, v26
	v_fma_f32 v23, v23, 4.0, 4.0
	v_mul_f32_e32 v24, v23, v24
	v_fmamk_f32 v23, v135, 0x39000000, v7
	v_mul_f32_e32 v26, v27, v26
	v_fmamk_f32 v27, v141, 0x39000000, v5
	v_min_f32_e32 v27, 0x40e00000, v27
	v_mul_f32_e32 v28, 0xc01d265f, v27
	v_med3_f32 v23, v23, s87, v224
	v_exp_f32_e32 v28, v28
	v_fma_f32 v23, v23, 4.0, 4.0
	v_mul_f32_e32 v25, v23, v25
	v_fmamk_f32 v23, v136, 0x39000000, v8
	v_med3_f32 v23, v23, s87, v224
	v_fma_f32 v23, v23, 4.0, 4.0
	v_add_f32_e32 v28, 1.0, v28
	v_mul_f32_e32 v26, v23, v26
	v_fmamk_f32 v23, v137, 0x39000000, v9
	v_rcp_f32_e32 v28, v28
	v_med3_f32 v29, v23, s87, v224
	v_mov_b32_e32 v23, 0
	v_cvt_pk_fp8_f32 v23, v24, v25
	v_mul_f32_e32 v24, v27, v28
	v_fma_f32 v25, v29, 4.0, 4.0
	v_mul_f32_e32 v24, v25, v24
	v_cvt_pk_fp8_f32 v23, v26, v24 op_sel:[0,0,1]
	v_add_co_u32_e32 v24, vcc, 0x10000, v18
	v_permlane16_swap_b32_e32 v20, v22
	s_nop 0
	v_addc_co_u32_e32 v25, vcc, 0, v19, vcc
	v_permlane16_swap_b32_e32 v21, v23
	s_and_b64 vcc, exec, s[6:7]
	global_store_dwordx4 v[24:25], v[20:23], off sc1 nt
	s_cbranch_vccz .LBB0_1188
	s_andn2_b64 vcc, exec, s[52:53]
	s_cbranch_vccnz .LBB0_1189

.LBB0_1188:
	s_nop 0
	v_fmamk_f32 v20, v130, 0x39000000, v14
	v_min_f32_e32 v20, 0x40e00000, v20
	v_mul_f32_e32 v21, 0xc01d265f, v20
	v_exp_f32_e32 v21, v21
	v_fmamk_f32 v23, v131, 0x39000000, v15
	v_min_f32_e32 v23, 0x40e00000, v23
	v_mul_f32_e32 v24, 0xc01d265f, v23
	v_add_f32_e32 v21, 1.0, v21
	v_rcp_f32_e32 v21, v21
	v_exp_f32_e32 v24, v24
	v_fmamk_f32 v22, v126, 0x39000000, v10
	v_med3_f32 v22, v22, s87, v224
	v_mul_f32_e32 v20, v20, v21
	v_fma_f32 v21, v22, 4.0, 4.0
	v_add_f32_e32 v22, 1.0, v24
	v_rcp_f32_e32 v22, v22
	v_fmamk_f32 v25, v133, 0x39000000, v17
	v_min_f32_e32 v25, 0x40e00000, v25
	v_mul_f32_e32 v26, 0xc01d265f, v25
	v_mul_f32_e32 v22, v23, v22
	v_fmamk_f32 v23, v132, 0x39000000, v16
	v_min_f32_e32 v23, 0x40e00000, v23
	v_mul_f32_e32 v24, 0xc01d265f, v23
	v_exp_f32_e32 v24, v24
	v_exp_f32_e32 v26, v26
	v_mul_f32_e32 v21, v21, v20
	v_fmamk_f32 v20, v127, 0x39000000, v11
	v_add_f32_e32 v24, 1.0, v24
	v_rcp_f32_e32 v24, v24
	v_med3_f32 v20, v20, s87, v224
	v_fma_f32 v20, v20, 4.0, 4.0
	v_mul_f32_e32 v22, v20, v22
	v_fmamk_f32 v20, v128, 0x39000000, v12
	v_mul_f32_e32 v23, v23, v24
	v_add_f32_e32 v24, 1.0, v26
	v_med3_f32 v20, v20, s87, v224
	v_rcp_f32_e32 v24, v24
	v_fma_f32 v20, v20, 4.0, 4.0
	v_mul_f32_e32 v23, v20, v23
	v_fmamk_f32 v20, v129, 0x39000000, v13
	v_med3_f32 v20, v20, s87, v224
	v_mul_f32_e32 v24, v25, v24
	v_fma_f32 v25, v20, 4.0, 4.0
	v_mov_b32_e32 v20, v66
	v_cvt_pk_fp8_f32 v20, v21, v22
	v_fmamk_f32 v21, v122, 0x39000000, v2
	v_min_f32_e32 v21, 0x40e00000, v21
	v_mul_f32_e32 v22, 0xc01d265f, v21
	v_exp_f32_e32 v22, v22
	v_mul_f32_e32 v24, v25, v24
	v_cvt_pk_fp8_f32 v20, v23, v24 op_sel:[0,0,1]
	v_fmamk_f32 v24, v123, 0x39000000, v3
	v_min_f32_e32 v24, 0x40e00000, v24
	v_add_f32_e32 v22, 1.0, v22
	v_mul_f32_e32 v25, 0xc01d265f, v24
	v_rcp_f32_e32 v22, v22
	v_exp_f32_e32 v25, v25
	v_fmamk_f32 v23, v118, 0x39000000, v6
	v_med3_f32 v23, v23, s87, v224
	v_mul_f32_e32 v21, v21, v22
	v_fma_f32 v22, v23, 4.0, 4.0
	v_add_f32_e32 v23, 1.0, v25
	v_rcp_f32_e32 v23, v23
	v_fmamk_f32 v26, v125, 0x39000000, v5
	v_min_f32_e32 v26, 0x40e00000, v26
	v_mul_f32_e32 v27, 0xc01d265f, v26
	v_mul_f32_e32 v23, v24, v23
	v_fmamk_f32 v24, v124, 0x39000000, v4
	v_min_f32_e32 v24, 0x40e00000, v24
	v_mul_f32_e32 v25, 0xc01d265f, v24
	v_exp_f32_e32 v25, v25
	v_exp_f32_e32 v27, v27
	v_mul_f32_e32 v22, v22, v21
	v_fmamk_f32 v21, v119, 0x39000000, v7
	v_add_f32_e32 v25, 1.0, v25
	v_rcp_f32_e32 v25, v25
	v_med3_f32 v21, v21, s87, v224
	v_fma_f32 v21, v21, 4.0, 4.0
	v_mul_f32_e32 v23, v21, v23
	v_fmamk_f32 v21, v120, 0x39000000, v8
	v_mul_f32_e32 v24, v24, v25
	v_add_f32_e32 v25, 1.0, v27
	v_med3_f32 v21, v21, s87, v224
	v_rcp_f32_e32 v25, v25
	v_fma_f32 v21, v21, 4.0, 4.0
	v_mul_f32_e32 v24, v21, v24
	v_fmamk_f32 v21, v121, 0x39000000, v9
	v_med3_f32 v21, v21, s87, v224
	v_mul_f32_e32 v25, v26, v25
	v_fma_f32 v26, v21, 4.0, 4.0
	v_mov_b32_e32 v21, v66
	v_cvt_pk_fp8_f32 v21, v22, v23
	v_fmamk_f32 v22, v114, 0x39000000, v14
	v_min_f32_e32 v22, 0x40e00000, v22
	v_mul_f32_e32 v23, 0xc01d265f, v22
	v_exp_f32_e32 v23, v23
	v_mul_f32_e32 v25, v26, v25
	v_cvt_pk_fp8_f32 v21, v24, v25 op_sel:[0,0,1]
	v_fmamk_f32 v25, v115, 0x39000000, v15
	v_min_f32_e32 v25, 0x40e00000, v25
	v_add_f32_e32 v23, 1.0, v23
	v_mul_f32_e32 v26, 0xc01d265f, v25
	v_rcp_f32_e32 v23, v23
	v_exp_f32_e32 v26, v26
	v_fmamk_f32 v24, v110, 0x39000000, v10
	v_med3_f32 v24, v24, s87, v224
	v_mul_f32_e32 v22, v22, v23
	v_fma_f32 v23, v24, 4.0, 4.0
	v_add_f32_e32 v24, 1.0, v26
	v_rcp_f32_e32 v24, v24
	v_fmamk_f32 v27, v117, 0x39000000, v17
	v_min_f32_e32 v27, 0x40e00000, v27
	v_mul_f32_e32 v28, 0xc01d265f, v27
	v_mul_f32_e32 v24, v25, v24
	v_fmamk_f32 v25, v116, 0x39000000, v16
	v_min_f32_e32 v25, 0x40e00000, v25
	v_mul_f32_e32 v26, 0xc01d265f, v25
	v_exp_f32_e32 v26, v26
	v_exp_f32_e32 v28, v28
	v_mul_f32_e32 v23, v23, v22
	v_fmamk_f32 v22, v111, 0x39000000, v11
	v_add_f32_e32 v26, 1.0, v26
	v_rcp_f32_e32 v26, v26
	v_med3_f32 v22, v22, s87, v224
	v_fma_f32 v22, v22, 4.0, 4.0
	v_mul_f32_e32 v24, v22, v24
	v_fmamk_f32 v22, v112, 0x39000000, v12
	v_mul_f32_e32 v25, v25, v26
	v_add_f32_e32 v26, 1.0, v28
	v_med3_f32 v22, v22, s87, v224
	v_rcp_f32_e32 v26, v26
	v_fma_f32 v22, v22, 4.0, 4.0
	v_mul_f32_e32 v25, v22, v25
	v_fmamk_f32 v22, v113, 0x39000000, v13
	v_med3_f32 v22, v22, s87, v224
	v_mul_f32_e32 v26, v27, v26
	v_fma_f32 v27, v22, 4.0, 4.0
	v_fmamk_f32 v22, v106, 0x39000000, v2
	v_min_f32_e32 v28, 0x40e00000, v22
	v_mul_f32_e32 v22, 0xc01d265f, v28
	v_exp_f32_e32 v29, v22
	v_mov_b32_e32 v22, v66
	v_cvt_pk_fp8_f32 v22, v23, v24
	v_mul_f32_e32 v23, v27, v26
	v_add_f32_e32 v24, 1.0, v29
	v_rcp_f32_e32 v24, v24
	v_cvt_pk_fp8_f32 v22, v25, v23 op_sel:[0,0,1]
	v_fmamk_f32 v25, v107, 0x39000000, v3
	v_min_f32_e32 v25, 0x40e00000, v25
	v_mul_f32_e32 v26, 0xc01d265f, v25
	v_exp_f32_e32 v26, v26
	v_fmamk_f32 v27, v108, 0x39000000, v4
	v_min_f32_e32 v27, 0x40e00000, v27
	v_mul_f32_e32 v24, v28, v24
	v_add_f32_e32 v26, 1.0, v26
	v_mul_f32_e32 v28, 0xc01d265f, v27
	v_rcp_f32_e32 v26, v26
	v_exp_f32_e32 v28, v28
	v_fmamk_f32 v23, v102, 0x39000000, v6
	v_med3_f32 v23, v23, s87, v224
	v_mul_f32_e32 v25, v25, v26
	v_add_f32_e32 v26, 1.0, v28
	v_rcp_f32_e32 v26, v26
	v_fma_f32 v23, v23, 4.0, 4.0
	v_mul_f32_e32 v24, v23, v24
	v_fmamk_f32 v23, v103, 0x39000000, v7
	v_mul_f32_e32 v26, v27, v26
	v_fmamk_f32 v27, v109, 0x39000000, v5
	v_min_f32_e32 v27, 0x40e00000, v27
	v_mul_f32_e32 v28, 0xc01d265f, v27
	v_med3_f32 v23, v23, s87, v224
	v_exp_f32_e32 v28, v28
	v_fma_f32 v23, v23, 4.0, 4.0
	v_mul_f32_e32 v25, v23, v25
	v_fmamk_f32 v23, v104, 0x39000000, v8
	v_med3_f32 v23, v23, s87, v224
	v_fma_f32 v23, v23, 4.0, 4.0
	v_add_f32_e32 v28, 1.0, v28
	v_mul_f32_e32 v26, v23, v26
	v_fmamk_f32 v23, v105, 0x39000000, v9
	v_rcp_f32_e32 v28, v28
	v_med3_f32 v29, v23, s87, v224
	v_mov_b32_e32 v23, v66
	v_cvt_pk_fp8_f32 v23, v24, v25
	v_mul_f32_e32 v24, v27, v28
	v_fma_f32 v25, v29, 4.0, 4.0
	v_mul_f32_e32 v24, v25, v24
	v_cvt_pk_fp8_f32 v23, v26, v24 op_sel:[0,0,1]
	v_fmamk_f32 v24, v98, 0x39000000, v14
	v_min_f32_e32 v26, 0x40e00000, v24
	v_mul_f32_e32 v24, 0xc01d265f, v26
	v_exp_f32_e32 v27, v24
	v_add_co_u32_e32 v24, vcc, s89, v18
	v_permlane16_swap_b32_e32 v20, v22
	v_permlane16_swap_b32_e32 v21, v23
	v_addc_co_u32_e32 v25, vcc, 0, v19, vcc
	global_store_dwordx4 v[24:25], v[20:23], off sc1 nt
	v_fmamk_f32 v25, v101, 0x39000000, v17
	v_min_f32_e32 v25, 0x40e00000, v25
	v_fmamk_f32 v22, v99, 0x39000000, v15
	v_min_f32_e32 v22, 0x40e00000, v22
	v_mul_f32_e32 v23, 0xc01d265f, v22
	v_exp_f32_e32 v23, v23
	v_add_f32_e32 v21, 1.0, v27
	v_rcp_f32_e32 v21, v21
	v_fmamk_f32 v20, v94, 0x39000000, v10
	v_add_f32_e32 v23, 1.0, v23
	v_rcp_f32_e32 v23, v23
	v_med3_f32 v20, v20, s87, v224
	v_mul_f32_e32 v21, v26, v21
	v_mul_f32_e32 v26, 0xc01d265f, v25
	v_mul_f32_e32 v22, v22, v23
	v_fmamk_f32 v23, v100, 0x39000000, v16
	v_min_f32_e32 v23, 0x40e00000, v23
	v_mul_f32_e32 v24, 0xc01d265f, v23
	v_exp_f32_e32 v24, v24
	v_fma_f32 v20, v20, 4.0, 4.0
	v_exp_f32_e32 v26, v26
	v_mul_f32_e32 v21, v20, v21
	v_add_f32_e32 v24, 1.0, v24
	v_rcp_f32_e32 v24, v24
	v_fmamk_f32 v20, v95, 0x39000000, v11
	v_med3_f32 v20, v20, s87, v224
	v_fma_f32 v20, v20, 4.0, 4.0
	v_mul_f32_e32 v22, v20, v22
	v_fmamk_f32 v20, v96, 0x39000000, v12
	v_mul_f32_e32 v23, v23, v24
	v_add_f32_e32 v24, 1.0, v26
	v_med3_f32 v20, v20, s87, v224
	v_rcp_f32_e32 v24, v24
	v_fma_f32 v20, v20, 4.0, 4.0
	v_mul_f32_e32 v23, v20, v23
	v_fmamk_f32 v20, v97, 0x39000000, v13
	v_med3_f32 v20, v20, s87, v224
	v_mul_f32_e32 v24, v25, v24
	v_fma_f32 v25, v20, 4.0, 4.0
	v_mov_b32_e32 v20, v66
	v_cvt_pk_fp8_f32 v20, v21, v22
	v_fmamk_f32 v21, v90, 0x39000000, v2
	v_min_f32_e32 v21, 0x40e00000, v21
	v_mul_f32_e32 v22, 0xc01d265f, v21
	v_exp_f32_e32 v22, v22
	v_mul_f32_e32 v24, v25, v24
	v_cvt_pk_fp8_f32 v20, v23, v24 op_sel:[0,0,1]
	v_fmamk_f32 v24, v91, 0x39000000, v3
	v_min_f32_e32 v24, 0x40e00000, v24
	v_add_f32_e32 v22, 1.0, v22
	v_mul_f32_e32 v25, 0xc01d265f, v24
	v_rcp_f32_e32 v22, v22
	v_exp_f32_e32 v25, v25
	v_fmamk_f32 v23, v86, 0x39000000, v6
	v_med3_f32 v23, v23, s87, v224
	v_mul_f32_e32 v21, v21, v22
	v_fma_f32 v22, v23, 4.0, 4.0
	v_add_f32_e32 v23, 1.0, v25
	v_rcp_f32_e32 v23, v23
	v_fmamk_f32 v26, v93, 0x39000000, v5
	v_min_f32_e32 v26, 0x40e00000, v26
	v_mul_f32_e32 v27, 0xc01d265f, v26
	v_mul_f32_e32 v23, v24, v23
	v_fmamk_f32 v24, v92, 0x39000000, v4
	v_min_f32_e32 v24, 0x40e00000, v24
	v_mul_f32_e32 v25, 0xc01d265f, v24
	v_exp_f32_e32 v25, v25
	v_exp_f32_e32 v27, v27
	v_mul_f32_e32 v22, v22, v21
	v_fmamk_f32 v21, v87, 0x39000000, v7
	v_add_f32_e32 v25, 1.0, v25
	v_rcp_f32_e32 v25, v25
	v_med3_f32 v21, v21, s87, v224
	v_fma_f32 v21, v21, 4.0, 4.0
	v_mul_f32_e32 v23, v21, v23
	v_fmamk_f32 v21, v88, 0x39000000, v8
	v_mul_f32_e32 v24, v24, v25
	v_add_f32_e32 v25, 1.0, v27
	v_med3_f32 v21, v21, s87, v224
	v_rcp_f32_e32 v25, v25
	v_fma_f32 v21, v21, 4.0, 4.0
	v_mul_f32_e32 v24, v21, v24
	v_fmamk_f32 v21, v89, 0x39000000, v9
	v_med3_f32 v21, v21, s87, v224
	v_fmamk_f32 v14, v82, 0x39000000, v14
	v_mul_f32_e32 v25, v26, v25
	v_fma_f32 v26, v21, 4.0, 4.0
	v_mov_b32_e32 v21, v66
	v_min_f32_e32 v14, 0x40e00000, v14
	v_cvt_pk_fp8_f32 v21, v22, v23
	v_mul_f32_e32 v22, 0xc01d265f, v14
	v_exp_f32_e32 v22, v22
	v_fmamk_f32 v15, v83, 0x39000000, v15
	v_mul_f32_e32 v23, v26, v25
	v_min_f32_e32 v15, 0x40e00000, v15
	v_cvt_pk_fp8_f32 v21, v24, v23 op_sel:[0,0,1]
	v_add_f32_e32 v22, 1.0, v22
	v_mul_f32_e32 v23, 0xc01d265f, v15
	v_rcp_f32_e32 v22, v22
	v_exp_f32_e32 v23, v23
	v_fmamk_f32 v10, v78, 0x39000000, v10
	v_med3_f32 v10, v10, s87, v224
	v_mul_f32_e32 v14, v14, v22
	v_add_f32_e32 v22, 1.0, v23
	v_rcp_f32_e32 v22, v22
	v_fma_f32 v10, v10, 4.0, 4.0
	v_mul_f32_e32 v10, v10, v14
	v_fmamk_f32 v11, v79, 0x39000000, v11
	v_mul_f32_e32 v14, v15, v22
	v_fmamk_f32 v15, v84, 0x39000000, v16
	v_min_f32_e32 v15, 0x40e00000, v15
	v_mul_f32_e32 v16, 0xc01d265f, v15
	v_exp_f32_e32 v16, v16
	v_med3_f32 v11, v11, s87, v224
	v_fma_f32 v11, v11, 4.0, 4.0
	v_fmac_f32_e32 v17, 0x39000000, v85
	v_mul_f32_e32 v11, v11, v14
	v_add_f32_e32 v14, 1.0, v16
	v_min_f32_e32 v16, 0x40e00000, v17
	v_mul_f32_e32 v17, 0xc01d265f, v16
	v_rcp_f32_e32 v14, v14
	v_exp_f32_e32 v17, v17
	v_fmamk_f32 v12, v80, 0x39000000, v12
	v_med3_f32 v12, v12, s87, v224
	v_mul_f32_e32 v14, v15, v14
	v_add_f32_e32 v15, 1.0, v17
	v_rcp_f32_e32 v15, v15
	v_fmamk_f32 v2, v74, 0x39000000, v2
	v_fma_f32 v12, v12, 4.0, 4.0
	v_min_f32_e32 v2, 0x40e00000, v2
	v_mul_f32_e32 v12, v12, v14
	v_mul_f32_e32 v14, v16, v15
	v_mul_f32_e32 v15, 0xc01d265f, v2
	v_exp_f32_e32 v15, v15
	v_mov_b32_e32 v22, v66
	v_fmac_f32_e32 v13, 0x39000000, v81
	v_cvt_pk_fp8_f32 v22, v10, v11
	v_med3_f32 v13, v13, s87, v224
	v_fma_f32 v13, v13, 4.0, 4.0
	v_fmamk_f32 v3, v75, 0x39000000, v3
	v_mul_f32_e32 v10, v13, v14
	v_add_f32_e32 v11, 1.0, v15
	v_min_f32_e32 v3, 0x40e00000, v3
	v_rcp_f32_e32 v11, v11
	v_cvt_pk_fp8_f32 v22, v12, v10 op_sel:[0,0,1]
	v_mul_f32_e32 v10, 0xc01d265f, v3
	v_exp_f32_e32 v10, v10
	v_fmamk_f32 v6, v70, 0x39000000, v6
	v_med3_f32 v6, v6, s87, v224
	v_fmamk_f32 v4, v76, 0x39000000, v4
	v_mul_f32_e32 v2, v2, v11
	v_fma_f32 v6, v6, 4.0, 4.0
	v_min_f32_e32 v4, 0x40e00000, v4
	v_mul_f32_e32 v2, v6, v2
	v_fmamk_f32 v6, v71, 0x39000000, v7
	v_add_f32_e32 v7, 1.0, v10
	v_mul_f32_e32 v10, 0xc01d265f, v4
	v_rcp_f32_e32 v7, v7
	v_exp_f32_e32 v10, v10
	v_fmac_f32_e32 v5, 0x39000000, v77
	v_min_f32_e32 v5, 0x40e00000, v5
	v_mul_f32_e32 v3, v3, v7
	v_add_f32_e32 v7, 1.0, v10
	v_rcp_f32_e32 v7, v7
	v_med3_f32 v6, v6, s87, v224
	v_fma_f32 v6, v6, 4.0, 4.0
	v_mul_f32_e32 v3, v6, v3
	v_mul_f32_e32 v4, v4, v7
	v_mul_f32_e32 v7, 0xc01d265f, v5
	v_exp_f32_e32 v7, v7
	v_fmamk_f32 v6, v72, 0x39000000, v8
	v_med3_f32 v6, v6, s87, v224
	v_fma_f32 v6, v6, 4.0, 4.0
	v_mul_f32_e32 v4, v6, v4
	v_add_f32_e32 v6, 1.0, v7
	v_rcp_f32_e32 v6, v6
	v_mov_b32_e32 v23, v66
	v_fmac_f32_e32 v9, 0x39000000, v73
	v_cvt_pk_fp8_f32 v23, v2, v3
	v_med3_f32 v7, v9, s87, v224
	v_mul_f32_e32 v2, v5, v6
	v_fma_f32 v3, v7, 4.0, 4.0
	v_mul_f32_e32 v2, v3, v2
	v_cvt_pk_fp8_f32 v23, v4, v2 op_sel:[0,0,1]
	v_add_co_u32_e32 v2, vcc, 0x50000, v18
	v_permlane16_swap_b32_e32 v20, v22
	v_permlane16_swap_b32_e32 v21, v23
	v_addc_co_u32_e32 v3, vcc, 0, v19, vcc
	global_store_dwordx4 v[2:3], v[20:23], off sc1 nt
	s_andn2_b64 vcc, exec, s[52:53]
	s_cbranch_vccz .LBB0_1184

.LBB0_1306:
	s_lshl_b32 s8, s87, 10
	s_and_b32 s8, s8, 0x400
	v_add_u32_e32 v10, s8, v1
	ds_read_b128 v[2:5], v10
	ds_read_b128 v[6:9], v10 offset:16
	ds_read_b128 v[20:23], v10 offset:512
	ds_read_b128 v[24:27], v10 offset:528
	v_lshl_add_u32 v12, s62, 8, v217
	s_waitcnt lgkmcnt(0)
	v_pk_mul_f32 v[18:19], v[2:3], s[54:55] op_sel_hi:[1,0]
	v_pk_mul_f32 v[10:11], v[8:9], s[54:55] op_sel_hi:[1,0]
	v_pk_mul_f32 v[8:9], v[20:21], s[54:55] op_sel_hi:[1,0]
	v_lshlrev_b32_e32 v20, 8, v216
	v_and_b32_e32 v66, 0x700, v20
	v_pk_fma_f32 v[20:21], v[194:195], s[56:57], v[18:19] op_sel_hi:[1,0,1]
	v_pk_mul_f32 v[14:15], v[6:7], s[54:55] op_sel_hi:[1,0]
	v_pk_mul_f32 v[6:7], v[22:23], s[54:55] op_sel_hi:[1,0]
	v_med3_f32 v22, v20, s35, v234
	v_med3_f32 v21, v21, s35, v234
	v_mov_b32_e32 v20, v67
	v_cvt_pk_fp8_f32 v20, v22, v21
	v_pk_mul_f32 v[16:17], v[4:5], s[54:55] op_sel_hi:[1,0]
	v_pk_mul_f32 v[4:5], v[24:25], s[54:55] op_sel_hi:[1,0]
	v_pk_fma_f32 v[22:23], v[196:197], s[56:57], v[16:17] op_sel_hi:[1,0,1]
	v_ashrrev_i32_e32 v13, 31, v12
	v_med3_f32 v21, v22, s35, v234
	v_med3_f32 v22, v23, s35, v234
	v_cvt_pk_fp8_f32 v20, v21, v22 op_sel:[0,0,1]
	v_pk_fma_f32 v[22:23], v[190:191], s[56:57], v[14:15] op_sel_hi:[1,0,1]
	v_mov_b32_e32 v21, v67
	v_med3_f32 v22, v22, s35, v234
	v_med3_f32 v23, v23, s35, v234
	v_cvt_pk_fp8_f32 v21, v22, v23
	v_pk_fma_f32 v[22:23], v[192:193], s[56:57], v[10:11] op_sel_hi:[1,0,1]
	v_lshlrev_b64 v[12:13], 11, v[12:13]
	v_med3_f32 v22, v22, s35, v234
	v_med3_f32 v23, v23, s35, v234
	v_cvt_pk_fp8_f32 v21, v22, v23 op_sel:[0,0,1]
	v_pk_fma_f32 v[22:23], v[186:187], s[56:57], v[18:19] op_sel_hi:[1,0,1]
	v_lshl_add_u64 v[12:13], s[44:45], 0, v[12:13]
	v_med3_f32 v24, v22, s35, v234
	v_med3_f32 v23, v23, s35, v234
	v_mov_b32_e32 v22, v67
	v_cvt_pk_fp8_f32 v22, v24, v23
	v_pk_fma_f32 v[24:25], v[188:189], s[56:57], v[16:17] op_sel_hi:[1,0,1]
	v_lshl_add_u64 v[12:13], v[12:13], 0, v[66:67]
	v_med3_f32 v23, v24, s35, v234
	v_med3_f32 v24, v25, s35, v234
	v_cvt_pk_fp8_f32 v22, v23, v24 op_sel:[0,0,1]
	v_pk_fma_f32 v[24:25], v[182:183], s[56:57], v[14:15] op_sel_hi:[1,0,1]
	v_mov_b32_e32 v23, v67
	v_med3_f32 v24, v24, s35, v234
	v_med3_f32 v25, v25, s35, v234
	v_cvt_pk_fp8_f32 v23, v24, v25
	v_pk_fma_f32 v[24:25], v[184:185], s[56:57], v[10:11] op_sel_hi:[1,0,1]
	v_lshl_add_u64 v[12:13], v[12:13], 0, s[40:41]
	v_med3_f32 v24, v24, s35, v234
	v_med3_f32 v25, v25, s35, v234
	v_cvt_pk_fp8_f32 v23, v24, v25 op_sel:[0,0,1]
	v_lshl_add_u64 v[12:13], v[12:13], 0, v[208:209]
	v_permlane16_swap_b32_e32 v20, v22
	v_permlane16_swap_b32_e32 v21, v23
	global_store_dwordx4 v[12:13], v[20:23], off sc1 nt
	v_pk_mul_f32 v[2:3], v[26:27], s[54:55] op_sel_hi:[1,0]
	s_nop 0
	v_pk_fma_f32 v[20:21], v[178:179], s[56:57], v[8:9] op_sel_hi:[1,0,1]
	s_nop 0
	v_med3_f32 v22, v20, s35, v234
	v_med3_f32 v21, v21, s35, v234
	v_mov_b32_e32 v20, v67
	v_cvt_pk_fp8_f32 v20, v22, v21
	v_pk_fma_f32 v[22:23], v[180:181], s[56:57], v[6:7] op_sel_hi:[1,0,1]
	s_nop 0
	v_med3_f32 v21, v22, s35, v234
	v_med3_f32 v22, v23, s35, v234
	v_cvt_pk_fp8_f32 v20, v21, v22 op_sel:[0,0,1]
	v_pk_fma_f32 v[22:23], v[174:175], s[56:57], v[4:5] op_sel_hi:[1,0,1]
	v_mov_b32_e32 v21, v67
	v_med3_f32 v22, v22, s35, v234
	v_med3_f32 v23, v23, s35, v234
	v_cvt_pk_fp8_f32 v21, v22, v23
	v_pk_fma_f32 v[22:23], v[176:177], s[56:57], v[2:3] op_sel_hi:[1,0,1]
	s_nop 0
	v_med3_f32 v22, v22, s35, v234
	v_med3_f32 v23, v23, s35, v234
	v_cvt_pk_fp8_f32 v21, v22, v23 op_sel:[0,0,1]
	v_pk_fma_f32 v[22:23], v[170:171], s[56:57], v[8:9] op_sel_hi:[1,0,1]
	s_nop 0
	v_med3_f32 v24, v22, s35, v234
	v_med3_f32 v23, v23, s35, v234
	v_mov_b32_e32 v22, v67
	v_cvt_pk_fp8_f32 v22, v24, v23
	v_pk_fma_f32 v[24:25], v[172:173], s[56:57], v[6:7] op_sel_hi:[1,0,1]
	s_nop 0
	v_med3_f32 v23, v24, s35, v234
	v_med3_f32 v24, v25, s35, v234
	v_cvt_pk_fp8_f32 v22, v23, v24 op_sel:[0,0,1]
	v_pk_fma_f32 v[24:25], v[162:163], s[56:57], v[4:5] op_sel_hi:[1,0,1]
	v_mov_b32_e32 v23, v67
	v_med3_f32 v24, v24, s35, v234
	v_med3_f32 v25, v25, s35, v234
	v_cvt_pk_fp8_f32 v23, v24, v25
	v_pk_fma_f32 v[24:25], v[164:165], s[56:57], v[2:3] op_sel_hi:[1,0,1]
	v_permlane16_swap_b32_e32 v20, v22
	v_med3_f32 v24, v24, s35, v234
	v_med3_f32 v25, v25, s35, v234
	v_cvt_pk_fp8_f32 v23, v24, v25 op_sel:[0,0,1]
	s_nop 1
	v_permlane16_swap_b32_e32 v21, v23
	global_store_dwordx4 v[12:13], v[20:23], off offset:128 sc1 nt
	s_nop 1
	v_pk_fma_f32 v[20:21], v[166:167], s[56:57], v[18:19] op_sel_hi:[1,0,1]
	s_nop 0
	v_med3_f32 v22, v20, s35, v234
	v_med3_f32 v21, v21, s35, v234
	v_mov_b32_e32 v20, v67
	v_cvt_pk_fp8_f32 v20, v22, v21
	v_pk_fma_f32 v[22:23], v[168:169], s[56:57], v[16:17] op_sel_hi:[1,0,1]
	s_nop 0
	v_med3_f32 v21, v22, s35, v234
	v_med3_f32 v22, v23, s35, v234
	v_cvt_pk_fp8_f32 v20, v21, v22 op_sel:[0,0,1]
	v_pk_fma_f32 v[22:23], v[158:159], s[56:57], v[14:15] op_sel_hi:[1,0,1]
	v_mov_b32_e32 v21, v67
	v_med3_f32 v22, v22, s35, v234
	v_med3_f32 v23, v23, s35, v234
	v_cvt_pk_fp8_f32 v21, v22, v23
	v_pk_fma_f32 v[22:23], v[160:161], s[56:57], v[10:11] op_sel_hi:[1,0,1]
	s_nop 0
	v_med3_f32 v22, v22, s35, v234
	v_med3_f32 v23, v23, s35, v234
	v_cvt_pk_fp8_f32 v21, v22, v23 op_sel:[0,0,1]
	v_pk_fma_f32 v[22:23], v[154:155], s[56:57], v[18:19] op_sel_hi:[1,0,1]
	s_nop 0
	v_med3_f32 v24, v22, s35, v234
	v_med3_f32 v23, v23, s35, v234
	v_mov_b32_e32 v22, v67
	v_cvt_pk_fp8_f32 v22, v24, v23
	v_pk_fma_f32 v[24:25], v[156:157], s[56:57], v[16:17] op_sel_hi:[1,0,1]
	s_nop 0
	v_med3_f32 v23, v24, s35, v234
	v_med3_f32 v24, v25, s35, v234
	v_cvt_pk_fp8_f32 v22, v23, v24 op_sel:[0,0,1]
	v_pk_fma_f32 v[24:25], v[150:151], s[56:57], v[14:15] op_sel_hi:[1,0,1]
	v_mov_b32_e32 v23, v67
	v_med3_f32 v24, v24, s35, v234
	v_med3_f32 v25, v25, s35, v234
	v_cvt_pk_fp8_f32 v23, v24, v25
	v_pk_fma_f32 v[24:25], v[152:153], s[56:57], v[10:11] op_sel_hi:[1,0,1]
	v_permlane16_swap_b32_e32 v20, v22
	v_med3_f32 v24, v24, s35, v234
	v_med3_f32 v25, v25, s35, v234
	v_cvt_pk_fp8_f32 v23, v24, v25 op_sel:[0,0,1]
	v_add_co_u32_e32 v24, vcc, s77, v12
	s_nop 0
	v_permlane16_swap_b32_e32 v21, v23
	v_addc_co_u32_e32 v25, vcc, 0, v13, vcc
	global_store_dwordx4 v[24:25], v[20:23], off sc1 nt
	s_and_b64 vcc, exec, s[10:11]
	s_nop 0
	v_pk_fma_f32 v[20:21], v[146:147], s[56:57], v[8:9] op_sel_hi:[1,0,1]
	s_nop 0
	v_med3_f32 v22, v20, s35, v234
	v_med3_f32 v21, v21, s35, v234
	v_mov_b32_e32 v20, v67
	v_cvt_pk_fp8_f32 v20, v22, v21
	v_pk_fma_f32 v[22:23], v[148:149], s[56:57], v[6:7] op_sel_hi:[1,0,1]
	s_nop 0
	v_med3_f32 v21, v22, s35, v234
	v_med3_f32 v22, v23, s35, v234
	v_cvt_pk_fp8_f32 v20, v21, v22 op_sel:[0,0,1]
	v_pk_fma_f32 v[22:23], v[142:143], s[56:57], v[4:5] op_sel_hi:[1,0,1]
	v_mov_b32_e32 v21, v67
	v_med3_f32 v22, v22, s35, v234
	v_med3_f32 v23, v23, s35, v234
	v_cvt_pk_fp8_f32 v21, v22, v23
	v_pk_fma_f32 v[22:23], v[144:145], s[56:57], v[2:3] op_sel_hi:[1,0,1]
	s_nop 0
	v_med3_f32 v22, v22, s35, v234
	v_med3_f32 v23, v23, s35, v234
	v_cvt_pk_fp8_f32 v21, v22, v23 op_sel:[0,0,1]
	v_pk_fma_f32 v[22:23], v[138:139], s[56:57], v[8:9] op_sel_hi:[1,0,1]
	s_nop 0
	v_med3_f32 v26, v22, s35, v234
	v_med3_f32 v23, v23, s35, v234
	v_mov_b32_e32 v22, v67
	v_cvt_pk_fp8_f32 v22, v26, v23
	v_pk_fma_f32 v[26:27], v[140:141], s[56:57], v[6:7] op_sel_hi:[1,0,1]
	s_nop 0
	v_med3_f32 v23, v26, s35, v234
	v_med3_f32 v26, v27, s35, v234
	v_cvt_pk_fp8_f32 v22, v23, v26 op_sel:[0,0,1]
	v_pk_fma_f32 v[26:27], v[134:135], s[56:57], v[4:5] op_sel_hi:[1,0,1]
	v_mov_b32_e32 v23, v67
	v_med3_f32 v26, v26, s35, v234
	v_med3_f32 v27, v27, s35, v234
	v_cvt_pk_fp8_f32 v23, v26, v27
	v_pk_fma_f32 v[26:27], v[136:137], s[56:57], v[2:3] op_sel_hi:[1,0,1]
	v_permlane16_swap_b32_e32 v20, v22
	v_med3_f32 v26, v26, s35, v234
	v_med3_f32 v27, v27, s35, v234
	v_cvt_pk_fp8_f32 v23, v26, v27 op_sel:[0,0,1]
	s_nop 1
	v_permlane16_swap_b32_e32 v21, v23
	global_store_dwordx4 v[24:25], v[20:23], off offset:128 sc1 nt
	s_cbranch_vccz .LBB0_1312
	s_andn2_b64 vcc, exec, s[6:7]
	s_cbranch_vccnz .LBB0_1313

.LBB0_1312:
	s_nop 0
	v_pk_fma_f32 v[20:21], v[130:131], s[56:57], v[18:19] op_sel_hi:[1,0,1]
	s_nop 0
	v_med3_f32 v22, v20, s35, v234
	v_med3_f32 v21, v21, s35, v234
	v_mov_b32_e32 v20, v67
	v_cvt_pk_fp8_f32 v20, v22, v21
	v_pk_fma_f32 v[22:23], v[132:133], s[56:57], v[16:17] op_sel_hi:[1,0,1]
	s_nop 0
	v_med3_f32 v21, v22, s35, v234
	v_med3_f32 v22, v23, s35, v234
	v_cvt_pk_fp8_f32 v20, v21, v22 op_sel:[0,0,1]
	v_pk_fma_f32 v[22:23], v[126:127], s[56:57], v[14:15] op_sel_hi:[1,0,1]
	v_mov_b32_e32 v21, v67
	v_med3_f32 v22, v22, s35, v234
	v_med3_f32 v23, v23, s35, v234
	v_cvt_pk_fp8_f32 v21, v22, v23
	v_pk_fma_f32 v[22:23], v[128:129], s[56:57], v[10:11] op_sel_hi:[1,0,1]
	s_nop 0
	v_med3_f32 v22, v22, s35, v234
	v_med3_f32 v23, v23, s35, v234
	v_cvt_pk_fp8_f32 v21, v22, v23 op_sel:[0,0,1]
	v_pk_fma_f32 v[22:23], v[122:123], s[56:57], v[18:19] op_sel_hi:[1,0,1]
	s_nop 0
	v_med3_f32 v24, v22, s35, v234
	v_med3_f32 v23, v23, s35, v234
	v_mov_b32_e32 v22, v67
	v_cvt_pk_fp8_f32 v22, v24, v23
	v_pk_fma_f32 v[24:25], v[124:125], s[56:57], v[16:17] op_sel_hi:[1,0,1]
	s_nop 0
	v_med3_f32 v23, v24, s35, v234
	v_med3_f32 v24, v25, s35, v234
	v_cvt_pk_fp8_f32 v22, v23, v24 op_sel:[0,0,1]
	v_pk_fma_f32 v[24:25], v[118:119], s[56:57], v[14:15] op_sel_hi:[1,0,1]
	v_mov_b32_e32 v23, v67
	v_med3_f32 v24, v24, s35, v234
	v_med3_f32 v25, v25, s35, v234
	v_cvt_pk_fp8_f32 v23, v24, v25
	v_pk_fma_f32 v[24:25], v[120:121], s[56:57], v[10:11] op_sel_hi:[1,0,1]
	v_permlane16_swap_b32_e32 v20, v22
	v_med3_f32 v24, v24, s35, v234
	v_med3_f32 v25, v25, s35, v234
	v_cvt_pk_fp8_f32 v23, v24, v25 op_sel:[0,0,1]
	v_add_co_u32_e32 v24, vcc, s84, v12
	s_nop 0
	v_permlane16_swap_b32_e32 v21, v23
	v_addc_co_u32_e32 v25, vcc, 0, v13, vcc
	global_store_dwordx4 v[24:25], v[20:23], off sc1 nt
	s_nop 1
	v_pk_fma_f32 v[20:21], v[114:115], s[56:57], v[8:9] op_sel_hi:[1,0,1]
	s_nop 0
	v_med3_f32 v22, v20, s35, v234
	v_med3_f32 v21, v21, s35, v234
	v_mov_b32_e32 v20, v67
	v_cvt_pk_fp8_f32 v20, v22, v21
	v_pk_fma_f32 v[22:23], v[116:117], s[56:57], v[6:7] op_sel_hi:[1,0,1]
	s_nop 0
	v_med3_f32 v21, v22, s35, v234
	v_med3_f32 v22, v23, s35, v234
	v_cvt_pk_fp8_f32 v20, v21, v22 op_sel:[0,0,1]
	v_pk_fma_f32 v[22:23], v[110:111], s[56:57], v[4:5] op_sel_hi:[1,0,1]
	v_mov_b32_e32 v21, v67
	v_med3_f32 v22, v22, s35, v234
	v_med3_f32 v23, v23, s35, v234
	v_cvt_pk_fp8_f32 v21, v22, v23
	v_pk_fma_f32 v[22:23], v[112:113], s[56:57], v[2:3] op_sel_hi:[1,0,1]
	s_nop 0
	v_med3_f32 v22, v22, s35, v234
	v_med3_f32 v23, v23, s35, v234
	v_cvt_pk_fp8_f32 v21, v22, v23 op_sel:[0,0,1]
	v_pk_fma_f32 v[22:23], v[106:107], s[56:57], v[8:9] op_sel_hi:[1,0,1]
	s_nop 0
	v_med3_f32 v26, v22, s35, v234
	v_med3_f32 v23, v23, s35, v234
	v_mov_b32_e32 v22, v67
	v_cvt_pk_fp8_f32 v22, v26, v23
	v_pk_fma_f32 v[26:27], v[108:109], s[56:57], v[6:7] op_sel_hi:[1,0,1]
	s_nop 0
	v_med3_f32 v23, v26, s35, v234
	v_med3_f32 v26, v27, s35, v234
	v_cvt_pk_fp8_f32 v22, v23, v26 op_sel:[0,0,1]
	v_pk_fma_f32 v[26:27], v[102:103], s[56:57], v[4:5] op_sel_hi:[1,0,1]
	v_mov_b32_e32 v23, v67
	v_med3_f32 v26, v26, s35, v234
	v_med3_f32 v27, v27, s35, v234
	v_cvt_pk_fp8_f32 v23, v26, v27
	v_pk_fma_f32 v[26:27], v[104:105], s[56:57], v[2:3] op_sel_hi:[1,0,1]
	v_permlane16_swap_b32_e32 v20, v22
	v_med3_f32 v26, v26, s35, v234
	v_med3_f32 v27, v27, s35, v234
	v_cvt_pk_fp8_f32 v23, v26, v27 op_sel:[0,0,1]
	s_nop 1
	v_permlane16_swap_b32_e32 v21, v23
	global_store_dwordx4 v[24:25], v[20:23], off offset:128 sc1 nt
	s_nop 1
	v_pk_fma_f32 v[20:21], v[98:99], s[56:57], v[18:19] op_sel_hi:[1,0,1]
	v_pk_fma_f32 v[18:19], v[90:91], s[56:57], v[18:19] op_sel_hi:[1,0,1]
	v_med3_f32 v22, v20, s35, v234
	v_med3_f32 v21, v21, s35, v234
	v_mov_b32_e32 v20, v67
	v_cvt_pk_fp8_f32 v20, v22, v21
	v_pk_fma_f32 v[22:23], v[100:101], s[56:57], v[16:17] op_sel_hi:[1,0,1]
	v_med3_f32 v18, v18, s35, v234
	v_med3_f32 v21, v22, s35, v234
	v_med3_f32 v22, v23, s35, v234
	v_cvt_pk_fp8_f32 v20, v21, v22 op_sel:[0,0,1]
	v_pk_fma_f32 v[22:23], v[94:95], s[56:57], v[14:15] op_sel_hi:[1,0,1]
	v_mov_b32_e32 v21, v67
	v_med3_f32 v22, v22, s35, v234
	v_med3_f32 v23, v23, s35, v234
	v_cvt_pk_fp8_f32 v21, v22, v23
	v_pk_fma_f32 v[22:23], v[96:97], s[56:57], v[10:11] op_sel_hi:[1,0,1]
	v_pk_fma_f32 v[14:15], v[86:87], s[56:57], v[14:15] op_sel_hi:[1,0,1]
	v_med3_f32 v22, v22, s35, v234
	v_med3_f32 v23, v23, s35, v234
	v_cvt_pk_fp8_f32 v21, v22, v23 op_sel:[0,0,1]
	v_med3_f32 v14, v14, s35, v234
	v_med3_f32 v15, v15, s35, v234
	v_mov_b32_e32 v23, v67
	v_cvt_pk_fp8_f32 v23, v14, v15
	v_pk_fma_f32 v[10:11], v[88:89], s[56:57], v[10:11] op_sel_hi:[1,0,1]
	v_add_co_u32_e32 v14, vcc, s85, v12
	v_med3_f32 v10, v10, s35, v234
	v_med3_f32 v11, v11, s35, v234
	v_cvt_pk_fp8_f32 v23, v10, v11 op_sel:[0,0,1]
	v_pk_fma_f32 v[10:11], v[82:83], s[56:57], v[8:9] op_sel_hi:[1,0,1]
	v_addc_co_u32_e32 v15, vcc, 0, v13, vcc
	v_med3_f32 v12, v10, s35, v234
	v_med3_f32 v11, v11, s35, v234
	v_mov_b32_e32 v10, v67
	v_cvt_pk_fp8_f32 v10, v12, v11
	v_pk_fma_f32 v[12:13], v[84:85], s[56:57], v[6:7] op_sel_hi:[1,0,1]
	v_pk_fma_f32 v[8:9], v[74:75], s[56:57], v[8:9] op_sel_hi:[1,0,1]
	v_med3_f32 v11, v12, s35, v234
	v_med3_f32 v12, v13, s35, v234
	v_cvt_pk_fp8_f32 v10, v11, v12 op_sel:[0,0,1]
	v_pk_fma_f32 v[12:13], v[78:79], s[56:57], v[4:5] op_sel_hi:[1,0,1]
	v_mov_b32_e32 v11, v67
	v_med3_f32 v12, v12, s35, v234
	v_med3_f32 v13, v13, s35, v234
	v_cvt_pk_fp8_f32 v11, v12, v13
	v_pk_fma_f32 v[12:13], v[80:81], s[56:57], v[2:3] op_sel_hi:[1,0,1]
	v_pk_fma_f32 v[4:5], v[70:71], s[56:57], v[4:5] op_sel_hi:[1,0,1]
	v_med3_f32 v12, v12, s35, v234
	v_med3_f32 v13, v13, s35, v234
	v_med3_f32 v19, v19, s35, v234
	v_mov_b32_e32 v22, v67
	v_cvt_pk_fp8_f32 v11, v12, v13 op_sel:[0,0,1]
	v_med3_f32 v8, v8, s35, v234
	v_med3_f32 v9, v9, s35, v234
	v_mov_b32_e32 v12, v67
	v_med3_f32 v4, v4, s35, v234
	v_med3_f32 v5, v5, s35, v234
	v_mov_b32_e32 v13, v67
	v_cvt_pk_fp8_f32 v22, v18, v19
	v_cvt_pk_fp8_f32 v12, v8, v9
	v_cvt_pk_fp8_f32 v13, v4, v5
	v_pk_fma_f32 v[16:17], v[92:93], s[56:57], v[16:17] op_sel_hi:[1,0,1]
	v_pk_fma_f32 v[6:7], v[76:77], s[56:57], v[6:7] op_sel_hi:[1,0,1]
	v_pk_fma_f32 v[2:3], v[72:73], s[56:57], v[2:3] op_sel_hi:[1,0,1]
	v_med3_f32 v16, v16, s35, v234
	v_med3_f32 v17, v17, s35, v234
	v_med3_f32 v6, v6, s35, v234
	v_med3_f32 v7, v7, s35, v234
	v_med3_f32 v2, v2, s35, v234
	v_med3_f32 v3, v3, s35, v234
	v_cvt_pk_fp8_f32 v22, v16, v17 op_sel:[0,0,1]
	v_cvt_pk_fp8_f32 v12, v6, v7 op_sel:[0,0,1]
	v_cvt_pk_fp8_f32 v13, v2, v3 op_sel:[0,0,1]
	v_permlane16_swap_b32_e32 v21, v23
	v_permlane16_swap_b32_e32 v20, v22
	v_permlane16_swap_b32_e32 v10, v12
	v_permlane16_swap_b32_e32 v11, v13
	global_store_dwordx4 v[14:15], v[20:23], off sc1 nt
	global_store_dwordx4 v[14:15], v[10:13], off offset:128 sc1 nt
	s_andn2_b64 vcc, exec, s[6:7]
	s_cbranch_vccz .LBB0_1308
